# baseline (speedup 1.0000x reference)
_Z11center_mainPKfPKcS0_Pf:
	s_load_dwordx4 s[4:7], s[0:1], 0x0
	s_load_dwordx4 s[8:11], s[0:1], 0x10
	s_and_b32 s3, s2, 7
	s_lshr_b32 s12, s2, 3
	s_mov_b32 s30, s2
	v_lshrrev_b32_e32 v1, 6, v0
	v_and_b32_e32 v2, 63, v0
	v_bfe_u32 v3, v0, 3, 3
	v_and_b32_e32 v4, 7, v0
	v_lshrrev_b32_e32 v5, 7, v0
	v_bfe_u32 v6, v0, 6, 1
	v_lshl_or_b32 v7, v5, 3, v3
	v_lshlrev_b32_e32 v8, 10, v7
	v_lshl_or_b32 v8, v6, 9, v8
	v_lshl_or_b32 v226, v4, 4, v8
	v_lshlrev_b32_e32 v17, 15, v1
	v_lshl_or_b32 v227, v2, 5, v17
	v_lshlrev_b32_e32 v237, 3, v0
	s_lshl_b32 s13, s3, 22
	s_lshl_b32 s14, s12, 15
	s_add_u32 s13, s13, s14
	s_lshl_b32 s15, s3, 18
	s_lshl_b32 s28, s3, 12
	s_waitcnt lgkmcnt(0)
	s_add_u32 s16, s4, s13
	s_addc_u32 s17, s5, 0
	global_load_dwordx4 v[194:197], v226, s[16:17] offset:0 nt
	global_load_dwordx4 v[198:201], v226, s[16:17] offset:128 nt
	global_load_dwordx4 v[202:205], v226, s[16:17] offset:256 nt
	global_load_dwordx4 v[206:209], v226, s[16:17] offset:384 nt
	s_add_u32 s8, s8, s28
	s_addc_u32 s9, s9, 0
	global_load_dwordx2 v[238:239], v237, s[8:9]
	s_add_u32 s24, s6, s15
	s_addc_u32 s25, s7, 0
	s_add_u32 s32, s24, 0x1000
	s_addc_u32 s33, s25, 0
	s_add_u32 s34, s24, 0x2000
	s_addc_u32 s35, s25, 0
	s_add_u32 s36, s24, 0x3000
	s_addc_u32 s37, s25, 0
	s_add_u32 s38, s24, 0x4000
	s_addc_u32 s39, s25, 0
	s_add_u32 s40, s24, 0x5000
	s_addc_u32 s41, s25, 0
	s_add_u32 s42, s24, 0x6000
	s_addc_u32 s43, s25, 0
	s_add_u32 s44, s24, 0x7000
	s_addc_u32 s45, s25, 0
	global_load_dwordx4 v[34:37], v227, s[24:25] offset:0
	global_load_dwordx4 v[38:41], v227, s[24:25] offset:16
	global_load_dwordx4 v[26:29], v227, s[24:25] offset:2048
	global_load_dwordx4 v[30:33], v227, s[24:25] offset:2064
	global_load_dwordx4 v[50:53], v227, s[32:33] offset:0
	global_load_dwordx4 v[54:57], v227, s[32:33] offset:16
	global_load_dwordx4 v[42:45], v227, s[32:33] offset:2048
	global_load_dwordx4 v[46:49], v227, s[32:33] offset:2064
	global_load_dwordx4 v[18:21], v227, s[34:35] offset:0
	global_load_dwordx4 v[22:25], v227, s[34:35] offset:16
	global_load_dwordx4 v[130:133], v227, s[34:35] offset:2048
	global_load_dwordx4 v[134:137], v227, s[34:35] offset:2064
	global_load_dwordx4 v[122:125], v227, s[36:37] offset:0
	global_load_dwordx4 v[126:129], v227, s[36:37] offset:16
	global_load_dwordx4 v[138:141], v227, s[36:37] offset:2048
	global_load_dwordx4 v[142:145], v227, s[36:37] offset:2064
	global_load_dwordx4 v[98:101], v227, s[38:39] offset:0
	global_load_dwordx4 v[102:105], v227, s[38:39] offset:16
	global_load_dwordx4 v[90:93], v227, s[38:39] offset:2048
	global_load_dwordx4 v[94:97], v227, s[38:39] offset:2064
	global_load_dwordx4 v[114:117], v227, s[40:41] offset:0
	global_load_dwordx4 v[118:121], v227, s[40:41] offset:16
	global_load_dwordx4 v[106:109], v227, s[40:41] offset:2048
	global_load_dwordx4 v[110:113], v227, s[40:41] offset:2064
	global_load_dwordx4 v[58:61], v227, s[42:43] offset:0
	global_load_dwordx4 v[62:65], v227, s[42:43] offset:16
	global_load_dwordx4 v[66:69], v227, s[42:43] offset:2048
	global_load_dwordx4 v[70:73], v227, s[42:43] offset:2064
	global_load_dwordx4 v[74:77], v227, s[44:45] offset:0
	global_load_dwordx4 v[78:81], v227, s[44:45] offset:16
	global_load_dwordx4 v[82:85], v227, s[44:45] offset:2048
	global_load_dwordx4 v[86:89], v227, s[44:45] offset:2064
	s_add_u32 s18, s16, 0x100000
	s_addc_u32 s19, s17, 0
	s_add_u32 s20, s16, 0x200000
	s_addc_u32 s21, s17, 0
	s_add_u32 s22, s16, 0x300000
	s_addc_u32 s23, s17, 0
	v_mul_u32_u24_e32 v9, 0x110, v7
	v_lshl_add_u32 v9, v6, 7, v9
	v_lshl_add_u32 v228, v4, 4, v9
	v_lshlrev_b32_e32 v10, 6, v7
	v_lshl_or_b32 v10, v6, 5, v10
	v_lshl_or_b32 v229, v4, 2, v10
	v_and_b32_e32 v11, 31, v0
	v_bfe_u32 v12, v0, 5, 1
	v_mul_u32_u24_e32 v13, 0x110, v11
	v_lshl_add_u32 v230, v12, 5, v13
	v_lshlrev_b32_e32 v14, 9, v1
	v_lshl_or_b32 v231, v12, 4, v14
	v_xor_b32_e32 v15, 32, v2
	v_lshlrev_b32_e32 v232, 2, v15
	v_xor_b32_e32 v15, 16, v2
	v_lshlrev_b32_e32 v247, 2, v15
	v_lshlrev_b32_e32 v16, 7, v1
	v_lshl_or_b32 v233, v11, 2, v16
	v_mov_b32_e32 v234, 0x7f7f7f7f
	s_waitcnt vmcnt(32)
	ds_write_b64 v237, v[238:239] offset:34816
	v_mul_f32_e32 v244, v194, v194
	v_mul_f32_e32 v245, v198, v198
	v_cvt_pk_fp8_f32 v240, v194, v195
	v_cvt_pk_fp8_f32 v241, v198, v199
	v_cvt_pk_fp8_f32 v242, v202, v203
	v_cvt_pk_fp8_f32 v243, v206, v207
	v_fmac_f32_e32 v244, v195, v195
	v_fmac_f32_e32 v245, v199, v199
	v_fmac_f32_e32 v244, v196, v196
	v_fmac_f32_e32 v245, v200, v200
	v_fmac_f32_e32 v244, v197, v197
	v_fmac_f32_e32 v245, v201, v201
	v_fmac_f32_e32 v244, v202, v202
	v_fmac_f32_e32 v245, v206, v206
	v_fmac_f32_e32 v244, v203, v203
	v_fmac_f32_e32 v245, v207, v207
	v_fmac_f32_e32 v244, v204, v204
	v_fmac_f32_e32 v245, v208, v208
	v_fmac_f32_e32 v244, v205, v205
	v_fmac_f32_e32 v245, v209, v209
	v_cvt_pk_fp8_f32 v240, v196, v197 op_sel:[0,0,1]
	v_cvt_pk_fp8_f32 v241, v200, v201 op_sel:[0,0,1]
	v_cvt_pk_fp8_f32 v242, v204, v205 op_sel:[0,0,1]
	v_cvt_pk_fp8_f32 v243, v208, v209 op_sel:[0,0,1]
	v_add_f32_e32 v244, v244, v245
	s_nop 0
	ds_write_b128 v228, v[240:243] offset:0
	ds_write_b32 v229, v244 offset:38912
	global_load_dwordx4 v[210:213], v226, s[18:19] offset:0 nt
	global_load_dwordx4 v[214:217], v226, s[18:19] offset:128 nt
	global_load_dwordx4 v[218:221], v226, s[18:19] offset:256 nt
	global_load_dwordx4 v[222:225], v226, s[18:19] offset:384 nt
	s_waitcnt lgkmcnt(0)
	s_barrier
	ds_read_b128 v[162:165], v230 offset:0
	ds_read_b128 v[166:169], v230 offset:16
	ds_read_b128 v[2:5], v231 offset:34816
	ds_read_b128 v[6:9], v231 offset:34848
	ds_read_b128 v[10:13], v231 offset:34880
	ds_read_b128 v[14:17], v231 offset:34912
	ds_read_b128 v[170:173], v230 offset:64
	ds_read_b128 v[174:177], v230 offset:80
	ds_read_b128 v[178:181], v230 offset:128
	ds_read_b128 v[182:185], v230 offset:144
	ds_read_b128 v[186:189], v230 offset:192
	ds_read_b128 v[190:193], v230 offset:208
	s_waitcnt vmcnt(34) lgkmcnt(6)
	v_mfma_scale_f32_32x32x64_f8f6f4 v[2:17], v[34:41], v[162:169], v[2:17], v234, v234 op_sel_hi:[0,0,0]
	s_waitcnt vmcnt(32) lgkmcnt(4)
	v_mfma_scale_f32_32x32x64_f8f6f4 v[2:17], v[26:33], v[170:177], v[2:17], v234, v234 op_sel_hi:[0,0,0]
	s_waitcnt vmcnt(30) lgkmcnt(2)
	v_mfma_scale_f32_32x32x64_f8f6f4 v[2:17], v[50:57], v[178:185], v[2:17], v234, v234 op_sel_hi:[0,0,0]
	s_waitcnt vmcnt(28) lgkmcnt(0)
	v_mfma_scale_f32_32x32x64_f8f6f4 v[2:17], v[42:49], v[186:193], v[2:17], v234, v234 op_sel_hi:[0,0,0]
	ds_read_b128 v[146:149], v231 offset:34944
	ds_read_b128 v[150:153], v231 offset:34976
	ds_read_b128 v[154:157], v231 offset:35008
	ds_read_b128 v[158:161], v231 offset:35040
	s_waitcnt vmcnt(26) lgkmcnt(0)
	v_mfma_scale_f32_32x32x64_f8f6f4 v[146:161], v[18:25], v[162:169], v[146:161], v234, v234 op_sel_hi:[0,0,0]
	s_waitcnt vmcnt(24)
	v_mfma_scale_f32_32x32x64_f8f6f4 v[146:161], v[130:137], v[170:177], v[146:161], v234, v234 op_sel_hi:[0,0,0]
	s_waitcnt vmcnt(22)
	v_mfma_scale_f32_32x32x64_f8f6f4 v[146:161], v[122:129], v[178:185], v[146:161], v234, v234 op_sel_hi:[0,0,0]
	s_waitcnt vmcnt(20)
	v_mfma_scale_f32_32x32x64_f8f6f4 v[146:161], v[138:145], v[186:193], v[146:161], v234, v234 op_sel_hi:[0,0,0]
	v_min3_f32 v2, v2, v3, v4
	v_min3_f32 v5, v5, v6, v7
	v_min3_f32 v8, v8, v9, v10
	v_min3_f32 v11, v11, v12, v13
	v_min3_f32 v14, v14, v15, v16
	v_min3_f32 v2, v2, v5, v8
	v_min3_f32 v11, v11, v14, v17
	v_min_f32_e32 v235, v2, v11
	ds_read_b128 v[2:5], v231 offset:35072
	ds_read_b128 v[6:9], v231 offset:35104
	ds_read_b128 v[10:13], v231 offset:35136
	ds_read_b128 v[14:17], v231 offset:35168
	s_waitcnt vmcnt(18) lgkmcnt(0)
	v_mfma_scale_f32_32x32x64_f8f6f4 v[2:17], v[98:105], v[162:169], v[2:17], v234, v234 op_sel_hi:[0,0,0]
	s_waitcnt vmcnt(16)
	v_mfma_scale_f32_32x32x64_f8f6f4 v[2:17], v[90:97], v[170:177], v[2:17], v234, v234 op_sel_hi:[0,0,0]
	s_waitcnt vmcnt(14)
	v_mfma_scale_f32_32x32x64_f8f6f4 v[2:17], v[114:121], v[178:185], v[2:17], v234, v234 op_sel_hi:[0,0,0]
	s_waitcnt vmcnt(12)
	v_mfma_scale_f32_32x32x64_f8f6f4 v[2:17], v[106:113], v[186:193], v[2:17], v234, v234 op_sel_hi:[0,0,0]
	global_load_dwordx4 v[194:197], v226, s[20:21] offset:0 nt
	global_load_dwordx4 v[198:201], v226, s[20:21] offset:128 nt
	global_load_dwordx4 v[202:205], v226, s[20:21] offset:256 nt
	global_load_dwordx4 v[206:209], v226, s[20:21] offset:384 nt
	v_min3_f32 v146, v146, v147, v148
	v_min3_f32 v149, v149, v150, v151
	v_min3_f32 v152, v152, v153, v154
	v_min3_f32 v155, v155, v156, v157
	v_min3_f32 v158, v158, v159, v160
	v_min3_f32 v146, v146, v149, v152
	v_min3_f32 v155, v155, v158, v161
	v_min3_f32 v235, v235, v146, v155
	ds_read_b128 v[146:149], v231 offset:35200
	ds_read_b128 v[150:153], v231 offset:35232
	ds_read_b128 v[154:157], v231 offset:35264
	ds_read_b128 v[158:161], v231 offset:35296
	s_waitcnt vmcnt(14) lgkmcnt(0)
	v_mfma_scale_f32_32x32x64_f8f6f4 v[146:161], v[58:65], v[162:169], v[146:161], v234, v234 op_sel_hi:[0,0,0]
	s_waitcnt vmcnt(12)
	v_mfma_scale_f32_32x32x64_f8f6f4 v[146:161], v[66:73], v[170:177], v[146:161], v234, v234 op_sel_hi:[0,0,0]
	s_waitcnt vmcnt(10)
	v_mfma_scale_f32_32x32x64_f8f6f4 v[146:161], v[74:81], v[178:185], v[146:161], v234, v234 op_sel_hi:[0,0,0]
	s_waitcnt vmcnt(8)
	v_mfma_scale_f32_32x32x64_f8f6f4 v[146:161], v[82:89], v[186:193], v[146:161], v234, v234 op_sel_hi:[0,0,0]
	s_waitcnt vmcnt(4)
	v_mul_f32_e32 v244, v210, v210
	v_mul_f32_e32 v245, v214, v214
	v_cvt_pk_fp8_f32 v240, v210, v211
	v_cvt_pk_fp8_f32 v241, v214, v215
	v_cvt_pk_fp8_f32 v242, v218, v219
	v_cvt_pk_fp8_f32 v243, v222, v223
	v_fmac_f32_e32 v244, v211, v211
	v_fmac_f32_e32 v245, v215, v215
	v_fmac_f32_e32 v244, v212, v212
	v_fmac_f32_e32 v245, v216, v216
	v_fmac_f32_e32 v244, v213, v213
	v_fmac_f32_e32 v245, v217, v217
	v_fmac_f32_e32 v244, v218, v218
	v_fmac_f32_e32 v245, v222, v222
	v_fmac_f32_e32 v244, v219, v219
	v_fmac_f32_e32 v245, v223, v223
	v_fmac_f32_e32 v244, v220, v220
	v_fmac_f32_e32 v245, v224, v224
	v_fmac_f32_e32 v244, v221, v221
	v_fmac_f32_e32 v245, v225, v225
	v_cvt_pk_fp8_f32 v240, v212, v213 op_sel:[0,0,1]
	v_cvt_pk_fp8_f32 v241, v216, v217 op_sel:[0,0,1]
	v_cvt_pk_fp8_f32 v242, v220, v221 op_sel:[0,0,1]
	v_cvt_pk_fp8_f32 v243, v224, v225 op_sel:[0,0,1]
	v_add_f32_e32 v244, v244, v245
	s_nop 0
	ds_write_b128 v228, v[240:243] offset:8704
	ds_write_b32 v229, v244 offset:40960
	global_load_dwordx4 v[210:213], v226, s[22:23] offset:0 nt
	global_load_dwordx4 v[214:217], v226, s[22:23] offset:128 nt
	global_load_dwordx4 v[218:221], v226, s[22:23] offset:256 nt
	global_load_dwordx4 v[222:225], v226, s[22:23] offset:384 nt
	v_min3_f32 v2, v2, v3, v4
	v_min3_f32 v5, v5, v6, v7
	v_min3_f32 v8, v8, v9, v10
	v_min3_f32 v11, v11, v12, v13
	v_min3_f32 v14, v14, v15, v16
	v_min3_f32 v2, v2, v5, v8
	v_min3_f32 v11, v11, v14, v17
	v_min3_f32 v235, v235, v2, v11
	ds_read_b128 v[2:5], v231 offset:34816
	ds_read_b128 v[6:9], v231 offset:34848
	ds_read_b128 v[10:13], v231 offset:34880
	ds_read_b128 v[14:17], v231 offset:34912
	s_waitcnt lgkmcnt(0)
	s_barrier
	ds_read_b128 v[162:165], v230 offset:8704
	ds_read_b128 v[166:169], v230 offset:8720
	ds_read_b128 v[170:173], v230 offset:8768
	ds_read_b128 v[174:177], v230 offset:8784
	ds_read_b128 v[178:181], v230 offset:8832
	ds_read_b128 v[182:185], v230 offset:8848
	ds_read_b128 v[186:189], v230 offset:8896
	ds_read_b128 v[190:193], v230 offset:8912
	s_waitcnt lgkmcnt(6)
	v_mfma_scale_f32_32x32x64_f8f6f4 v[2:17], v[34:41], v[162:169], v[2:17], v234, v234 op_sel_hi:[0,0,0]
	s_waitcnt lgkmcnt(4)
	v_mfma_scale_f32_32x32x64_f8f6f4 v[2:17], v[26:33], v[170:177], v[2:17], v234, v234 op_sel_hi:[0,0,0]
	s_waitcnt lgkmcnt(2)
	v_mfma_scale_f32_32x32x64_f8f6f4 v[2:17], v[50:57], v[178:185], v[2:17], v234, v234 op_sel_hi:[0,0,0]
	s_waitcnt lgkmcnt(0)
	v_mfma_scale_f32_32x32x64_f8f6f4 v[2:17], v[42:49], v[186:193], v[2:17], v234, v234 op_sel_hi:[0,0,0]
	v_min3_f32 v146, v146, v147, v148
	v_min3_f32 v149, v149, v150, v151
	v_min3_f32 v152, v152, v153, v154
	v_min3_f32 v155, v155, v156, v157
	v_min3_f32 v158, v158, v159, v160
	v_min3_f32 v146, v146, v149, v152
	v_min3_f32 v155, v155, v158, v161
	v_min3_f32 v235, v235, v146, v155
	ds_bpermute_b32 v246, v232, v235
	s_waitcnt lgkmcnt(0)
	v_min_f32_e32 v246, v235, v246
	ds_write_b32 v233, v246 offset:47104
	ds_read_b128 v[146:149], v231 offset:34944
	ds_read_b128 v[150:153], v231 offset:34976
	ds_read_b128 v[154:157], v231 offset:35008
	ds_read_b128 v[158:161], v231 offset:35040
	s_waitcnt lgkmcnt(0)
	v_mfma_scale_f32_32x32x64_f8f6f4 v[146:161], v[18:25], v[162:169], v[146:161], v234, v234 op_sel_hi:[0,0,0]
	v_mfma_scale_f32_32x32x64_f8f6f4 v[146:161], v[130:137], v[170:177], v[146:161], v234, v234 op_sel_hi:[0,0,0]
	v_mfma_scale_f32_32x32x64_f8f6f4 v[146:161], v[122:129], v[178:185], v[146:161], v234, v234 op_sel_hi:[0,0,0]
	v_mfma_scale_f32_32x32x64_f8f6f4 v[146:161], v[138:145], v[186:193], v[146:161], v234, v234 op_sel_hi:[0,0,0]
	v_min3_f32 v2, v2, v3, v4
	v_min3_f32 v5, v5, v6, v7
	v_min3_f32 v8, v8, v9, v10
	v_min3_f32 v11, v11, v12, v13
	v_min3_f32 v14, v14, v15, v16
	v_min3_f32 v2, v2, v5, v8
	v_min3_f32 v11, v11, v14, v17
	v_min_f32_e32 v236, v2, v11
	ds_read_b128 v[2:5], v231 offset:35072
	ds_read_b128 v[6:9], v231 offset:35104
	ds_read_b128 v[10:13], v231 offset:35136
	ds_read_b128 v[14:17], v231 offset:35168
	s_waitcnt lgkmcnt(0)
	v_mfma_scale_f32_32x32x64_f8f6f4 v[2:17], v[98:105], v[162:169], v[2:17], v234, v234 op_sel_hi:[0,0,0]
	v_mfma_scale_f32_32x32x64_f8f6f4 v[2:17], v[90:97], v[170:177], v[2:17], v234, v234 op_sel_hi:[0,0,0]
	v_mfma_scale_f32_32x32x64_f8f6f4 v[2:17], v[114:121], v[178:185], v[2:17], v234, v234 op_sel_hi:[0,0,0]
	v_mfma_scale_f32_32x32x64_f8f6f4 v[2:17], v[106:113], v[186:193], v[2:17], v234, v234 op_sel_hi:[0,0,0]
	v_min3_f32 v146, v146, v147, v148
	v_min3_f32 v149, v149, v150, v151
	v_min3_f32 v152, v152, v153, v154
	v_min3_f32 v155, v155, v156, v157
	v_min3_f32 v158, v158, v159, v160
	v_min3_f32 v146, v146, v149, v152
	v_min3_f32 v155, v155, v158, v161
	v_min3_f32 v236, v236, v146, v155
	ds_read_b128 v[146:149], v231 offset:35200
	ds_read_b128 v[150:153], v231 offset:35232
	ds_read_b128 v[154:157], v231 offset:35264
	ds_read_b128 v[158:161], v231 offset:35296
	s_waitcnt lgkmcnt(0)
	v_mfma_scale_f32_32x32x64_f8f6f4 v[146:161], v[58:65], v[162:169], v[146:161], v234, v234 op_sel_hi:[0,0,0]
	v_mfma_scale_f32_32x32x64_f8f6f4 v[146:161], v[66:73], v[170:177], v[146:161], v234, v234 op_sel_hi:[0,0,0]
	v_mfma_scale_f32_32x32x64_f8f6f4 v[146:161], v[74:81], v[178:185], v[146:161], v234, v234 op_sel_hi:[0,0,0]
	v_mfma_scale_f32_32x32x64_f8f6f4 v[146:161], v[82:89], v[186:193], v[146:161], v234, v234 op_sel_hi:[0,0,0]
	s_waitcnt vmcnt(4)
	v_mul_f32_e32 v244, v194, v194
	v_mul_f32_e32 v245, v198, v198
	v_cvt_pk_fp8_f32 v240, v194, v195
	v_cvt_pk_fp8_f32 v241, v198, v199
	v_cvt_pk_fp8_f32 v242, v202, v203
	v_cvt_pk_fp8_f32 v243, v206, v207
	v_fmac_f32_e32 v244, v195, v195
	v_fmac_f32_e32 v245, v199, v199
	v_fmac_f32_e32 v244, v196, v196
	v_fmac_f32_e32 v245, v200, v200
	v_fmac_f32_e32 v244, v197, v197
	v_fmac_f32_e32 v245, v201, v201
	v_fmac_f32_e32 v244, v202, v202
	v_fmac_f32_e32 v245, v206, v206
	v_fmac_f32_e32 v244, v203, v203
	v_fmac_f32_e32 v245, v207, v207
	v_fmac_f32_e32 v244, v204, v204
	v_fmac_f32_e32 v245, v208, v208
	v_fmac_f32_e32 v244, v205, v205
	v_fmac_f32_e32 v245, v209, v209
	v_cvt_pk_fp8_f32 v240, v196, v197 op_sel:[0,0,1]
	v_cvt_pk_fp8_f32 v241, v200, v201 op_sel:[0,0,1]
	v_cvt_pk_fp8_f32 v242, v204, v205 op_sel:[0,0,1]
	v_cvt_pk_fp8_f32 v243, v208, v209 op_sel:[0,0,1]
	v_add_f32_e32 v244, v244, v245
	s_nop 0
	ds_write_b128 v228, v[240:243] offset:17408
	ds_write_b32 v229, v244 offset:43008
	v_min3_f32 v2, v2, v3, v4
	v_min3_f32 v5, v5, v6, v7
	v_min3_f32 v8, v8, v9, v10
	v_min3_f32 v11, v11, v12, v13
	v_min3_f32 v14, v14, v15, v16
	v_min3_f32 v2, v2, v5, v8
	v_min3_f32 v11, v11, v14, v17
	v_min3_f32 v236, v236, v2, v11
	ds_read_b128 v[2:5], v231 offset:34816
	ds_read_b128 v[6:9], v231 offset:34848
	ds_read_b128 v[10:13], v231 offset:34880
	ds_read_b128 v[14:17], v231 offset:34912
	s_waitcnt lgkmcnt(0)
	s_barrier
	ds_read_b128 v[162:165], v230 offset:17408
	ds_read_b128 v[166:169], v230 offset:17424
	ds_read_b128 v[170:173], v230 offset:17472
	ds_read_b128 v[174:177], v230 offset:17488
	ds_read_b128 v[178:181], v230 offset:17536
	ds_read_b128 v[182:185], v230 offset:17552
	ds_read_b128 v[186:189], v230 offset:17600
	ds_read_b128 v[190:193], v230 offset:17616
	s_waitcnt lgkmcnt(6)
	v_mfma_scale_f32_32x32x64_f8f6f4 v[2:17], v[34:41], v[162:169], v[2:17], v234, v234 op_sel_hi:[0,0,0]
	s_waitcnt lgkmcnt(4)
	v_mfma_scale_f32_32x32x64_f8f6f4 v[2:17], v[26:33], v[170:177], v[2:17], v234, v234 op_sel_hi:[0,0,0]
	s_waitcnt lgkmcnt(2)
	v_mfma_scale_f32_32x32x64_f8f6f4 v[2:17], v[50:57], v[178:185], v[2:17], v234, v234 op_sel_hi:[0,0,0]
	s_waitcnt lgkmcnt(0)
	v_mfma_scale_f32_32x32x64_f8f6f4 v[2:17], v[42:49], v[186:193], v[2:17], v234, v234 op_sel_hi:[0,0,0]
	v_min3_f32 v146, v146, v147, v148
	v_min3_f32 v149, v149, v150, v151
	v_min3_f32 v152, v152, v153, v154
	v_min3_f32 v155, v155, v156, v157
	v_min3_f32 v158, v158, v159, v160
	v_min3_f32 v146, v146, v149, v152
	v_min3_f32 v155, v155, v158, v161
	v_min3_f32 v236, v236, v146, v155
	ds_bpermute_b32 v246, v232, v236
	s_waitcnt lgkmcnt(0)
	v_min_f32_e32 v246, v236, v246
	ds_write_b32 v233, v246 offset:48128
	ds_read_b128 v[146:149], v231 offset:34944
	ds_read_b128 v[150:153], v231 offset:34976
	ds_read_b128 v[154:157], v231 offset:35008
	ds_read_b128 v[158:161], v231 offset:35040
	s_waitcnt lgkmcnt(0)
	v_mfma_scale_f32_32x32x64_f8f6f4 v[146:161], v[18:25], v[162:169], v[146:161], v234, v234 op_sel_hi:[0,0,0]
	v_mfma_scale_f32_32x32x64_f8f6f4 v[146:161], v[130:137], v[170:177], v[146:161], v234, v234 op_sel_hi:[0,0,0]
	v_mfma_scale_f32_32x32x64_f8f6f4 v[146:161], v[122:129], v[178:185], v[146:161], v234, v234 op_sel_hi:[0,0,0]
	v_mfma_scale_f32_32x32x64_f8f6f4 v[146:161], v[138:145], v[186:193], v[146:161], v234, v234 op_sel_hi:[0,0,0]
	v_min3_f32 v2, v2, v3, v4
	v_min3_f32 v5, v5, v6, v7
	v_min3_f32 v8, v8, v9, v10
	v_min3_f32 v11, v11, v12, v13
	v_min3_f32 v14, v14, v15, v16
	v_min3_f32 v2, v2, v5, v8
	v_min3_f32 v11, v11, v14, v17
	v_min_f32_e32 v235, v2, v11
	ds_read_b128 v[2:5], v231 offset:35072
	ds_read_b128 v[6:9], v231 offset:35104
	ds_read_b128 v[10:13], v231 offset:35136
	ds_read_b128 v[14:17], v231 offset:35168
	s_waitcnt lgkmcnt(0)
	v_mfma_scale_f32_32x32x64_f8f6f4 v[2:17], v[98:105], v[162:169], v[2:17], v234, v234 op_sel_hi:[0,0,0]
	v_mfma_scale_f32_32x32x64_f8f6f4 v[2:17], v[90:97], v[170:177], v[2:17], v234, v234 op_sel_hi:[0,0,0]
	v_mfma_scale_f32_32x32x64_f8f6f4 v[2:17], v[114:121], v[178:185], v[2:17], v234, v234 op_sel_hi:[0,0,0]
	v_mfma_scale_f32_32x32x64_f8f6f4 v[2:17], v[106:113], v[186:193], v[2:17], v234, v234 op_sel_hi:[0,0,0]
	v_min3_f32 v146, v146, v147, v148
	v_min3_f32 v149, v149, v150, v151
	v_min3_f32 v152, v152, v153, v154
	v_min3_f32 v155, v155, v156, v157
	v_min3_f32 v158, v158, v159, v160
	v_min3_f32 v146, v146, v149, v152
	v_min3_f32 v155, v155, v158, v161
	v_min3_f32 v235, v235, v146, v155
	ds_read_b128 v[146:149], v231 offset:35200
	ds_read_b128 v[150:153], v231 offset:35232
	ds_read_b128 v[154:157], v231 offset:35264
	ds_read_b128 v[158:161], v231 offset:35296
	s_waitcnt lgkmcnt(0)
	v_mfma_scale_f32_32x32x64_f8f6f4 v[146:161], v[58:65], v[162:169], v[146:161], v234, v234 op_sel_hi:[0,0,0]
	v_mfma_scale_f32_32x32x64_f8f6f4 v[146:161], v[66:73], v[170:177], v[146:161], v234, v234 op_sel_hi:[0,0,0]
	v_mfma_scale_f32_32x32x64_f8f6f4 v[146:161], v[74:81], v[178:185], v[146:161], v234, v234 op_sel_hi:[0,0,0]
	v_mfma_scale_f32_32x32x64_f8f6f4 v[146:161], v[82:89], v[186:193], v[146:161], v234, v234 op_sel_hi:[0,0,0]
	s_waitcnt vmcnt(0)
	v_mul_f32_e32 v244, v210, v210
	v_mul_f32_e32 v245, v214, v214
	v_cvt_pk_fp8_f32 v240, v210, v211
	v_cvt_pk_fp8_f32 v241, v214, v215
	v_cvt_pk_fp8_f32 v242, v218, v219
	v_cvt_pk_fp8_f32 v243, v222, v223
	v_fmac_f32_e32 v244, v211, v211
	v_fmac_f32_e32 v245, v215, v215
	v_fmac_f32_e32 v244, v212, v212
	v_fmac_f32_e32 v245, v216, v216
	v_fmac_f32_e32 v244, v213, v213
	v_fmac_f32_e32 v245, v217, v217
	v_fmac_f32_e32 v244, v218, v218
	v_fmac_f32_e32 v245, v222, v222
	v_fmac_f32_e32 v244, v219, v219
	v_fmac_f32_e32 v245, v223, v223
	v_fmac_f32_e32 v244, v220, v220
	v_fmac_f32_e32 v245, v224, v224
	v_fmac_f32_e32 v244, v221, v221
	v_fmac_f32_e32 v245, v225, v225
	v_cvt_pk_fp8_f32 v240, v212, v213 op_sel:[0,0,1]
	v_cvt_pk_fp8_f32 v241, v216, v217 op_sel:[0,0,1]
	v_cvt_pk_fp8_f32 v242, v220, v221 op_sel:[0,0,1]
	v_cvt_pk_fp8_f32 v243, v224, v225 op_sel:[0,0,1]
	v_add_f32_e32 v244, v244, v245
	s_nop 0
	ds_write_b128 v228, v[240:243] offset:26112
	ds_write_b32 v229, v244 offset:45056
	v_min3_f32 v2, v2, v3, v4
	v_min3_f32 v5, v5, v6, v7
	v_min3_f32 v8, v8, v9, v10
	v_min3_f32 v11, v11, v12, v13
	v_min3_f32 v14, v14, v15, v16
	v_min3_f32 v2, v2, v5, v8
	v_min3_f32 v11, v11, v14, v17
	v_min3_f32 v235, v235, v2, v11
	ds_read_b128 v[2:5], v231 offset:34816
	ds_read_b128 v[6:9], v231 offset:34848
	ds_read_b128 v[10:13], v231 offset:34880
	ds_read_b128 v[14:17], v231 offset:34912
	s_waitcnt lgkmcnt(0)
	s_barrier
	ds_read_b128 v[162:165], v230 offset:26112
	ds_read_b128 v[166:169], v230 offset:26128
	ds_read_b128 v[170:173], v230 offset:26176
	ds_read_b128 v[174:177], v230 offset:26192
	ds_read_b128 v[178:181], v230 offset:26240
	ds_read_b128 v[182:185], v230 offset:26256
	ds_read_b128 v[186:189], v230 offset:26304
	ds_read_b128 v[190:193], v230 offset:26320
	s_waitcnt lgkmcnt(6)
	v_mfma_scale_f32_32x32x64_f8f6f4 v[2:17], v[34:41], v[162:169], v[2:17], v234, v234 op_sel_hi:[0,0,0]
	s_waitcnt lgkmcnt(4)
	v_mfma_scale_f32_32x32x64_f8f6f4 v[2:17], v[26:33], v[170:177], v[2:17], v234, v234 op_sel_hi:[0,0,0]
	s_waitcnt lgkmcnt(2)
	v_mfma_scale_f32_32x32x64_f8f6f4 v[2:17], v[50:57], v[178:185], v[2:17], v234, v234 op_sel_hi:[0,0,0]
	s_waitcnt lgkmcnt(0)
	v_mfma_scale_f32_32x32x64_f8f6f4 v[2:17], v[42:49], v[186:193], v[2:17], v234, v234 op_sel_hi:[0,0,0]
	v_min3_f32 v146, v146, v147, v148
	v_min3_f32 v149, v149, v150, v151
	v_min3_f32 v152, v152, v153, v154
	v_min3_f32 v155, v155, v156, v157
	v_min3_f32 v158, v158, v159, v160
	v_min3_f32 v146, v146, v149, v152
	v_min3_f32 v155, v155, v158, v161
	v_min3_f32 v235, v235, v146, v155
	ds_bpermute_b32 v246, v232, v235
	s_waitcnt lgkmcnt(0)
	v_min_f32_e32 v246, v235, v246
	ds_write_b32 v233, v246 offset:49152
	ds_read_b128 v[146:149], v231 offset:34944
	ds_read_b128 v[150:153], v231 offset:34976
	ds_read_b128 v[154:157], v231 offset:35008
	ds_read_b128 v[158:161], v231 offset:35040
	s_waitcnt lgkmcnt(0)
	v_mfma_scale_f32_32x32x64_f8f6f4 v[146:161], v[18:25], v[162:169], v[146:161], v234, v234 op_sel_hi:[0,0,0]
	v_mfma_scale_f32_32x32x64_f8f6f4 v[146:161], v[130:137], v[170:177], v[146:161], v234, v234 op_sel_hi:[0,0,0]
	v_mfma_scale_f32_32x32x64_f8f6f4 v[146:161], v[122:129], v[178:185], v[146:161], v234, v234 op_sel_hi:[0,0,0]
	v_mfma_scale_f32_32x32x64_f8f6f4 v[146:161], v[138:145], v[186:193], v[146:161], v234, v234 op_sel_hi:[0,0,0]
	v_min3_f32 v2, v2, v3, v4
	v_min3_f32 v5, v5, v6, v7
	v_min3_f32 v8, v8, v9, v10
	v_min3_f32 v11, v11, v12, v13
	v_min3_f32 v14, v14, v15, v16
	v_min3_f32 v2, v2, v5, v8
	v_min3_f32 v11, v11, v14, v17
	v_min_f32_e32 v236, v2, v11
	ds_read_b128 v[2:5], v231 offset:35072
	ds_read_b128 v[6:9], v231 offset:35104
	ds_read_b128 v[10:13], v231 offset:35136
	ds_read_b128 v[14:17], v231 offset:35168
	s_waitcnt lgkmcnt(0)
	v_mfma_scale_f32_32x32x64_f8f6f4 v[2:17], v[98:105], v[162:169], v[2:17], v234, v234 op_sel_hi:[0,0,0]
	v_mfma_scale_f32_32x32x64_f8f6f4 v[2:17], v[90:97], v[170:177], v[2:17], v234, v234 op_sel_hi:[0,0,0]
	v_mfma_scale_f32_32x32x64_f8f6f4 v[2:17], v[114:121], v[178:185], v[2:17], v234, v234 op_sel_hi:[0,0,0]
	v_mfma_scale_f32_32x32x64_f8f6f4 v[2:17], v[106:113], v[186:193], v[2:17], v234, v234 op_sel_hi:[0,0,0]
	v_min3_f32 v146, v146, v147, v148
	v_min3_f32 v149, v149, v150, v151
	v_min3_f32 v152, v152, v153, v154
	v_min3_f32 v155, v155, v156, v157
	v_min3_f32 v158, v158, v159, v160
	v_min3_f32 v146, v146, v149, v152
	v_min3_f32 v155, v155, v158, v161
	v_min3_f32 v236, v236, v146, v155
	ds_read_b128 v[146:149], v231 offset:35200
	ds_read_b128 v[150:153], v231 offset:35232
	ds_read_b128 v[154:157], v231 offset:35264
	ds_read_b128 v[158:161], v231 offset:35296
	s_waitcnt lgkmcnt(0)
	v_mfma_scale_f32_32x32x64_f8f6f4 v[146:161], v[58:65], v[162:169], v[146:161], v234, v234 op_sel_hi:[0,0,0]
	v_mfma_scale_f32_32x32x64_f8f6f4 v[146:161], v[66:73], v[170:177], v[146:161], v234, v234 op_sel_hi:[0,0,0]
	v_mfma_scale_f32_32x32x64_f8f6f4 v[146:161], v[74:81], v[178:185], v[146:161], v234, v234 op_sel_hi:[0,0,0]
	v_mfma_scale_f32_32x32x64_f8f6f4 v[146:161], v[82:89], v[186:193], v[146:161], v234, v234 op_sel_hi:[0,0,0]
	v_cmp_gt_u32_e32 vcc, 0x80, v0
	s_and_saveexec_b64 s[34:35], vcc
	v_lshlrev_b32_e32 v36, 6, v0
	ds_read_b128 v[20:23], v36 offset:38912
	ds_read_b128 v[24:27], v36 offset:38928
	ds_read_b128 v[28:31], v36 offset:38944
	ds_read_b128 v[32:35], v36 offset:38960
	s_mov_b64 exec, s[34:35]
	v_min3_f32 v2, v2, v3, v4
	v_min3_f32 v5, v5, v6, v7
	v_min3_f32 v8, v8, v9, v10
	v_min3_f32 v11, v11, v12, v13
	v_min3_f32 v14, v14, v15, v16
	v_min3_f32 v2, v2, v5, v8
	v_min3_f32 v11, v11, v14, v17
	v_min3_f32 v236, v236, v2, v11
	s_nop 15
	v_min3_f32 v146, v146, v147, v148
	v_min3_f32 v149, v149, v150, v151
	v_min3_f32 v152, v152, v153, v154
	v_min3_f32 v155, v155, v156, v157
	v_min3_f32 v158, v158, v159, v160
	v_min3_f32 v146, v146, v149, v152
	v_min3_f32 v155, v155, v158, v161
	v_min3_f32 v236, v236, v146, v155
	ds_bpermute_b32 v246, v232, v236
	s_waitcnt lgkmcnt(0)
	v_min_f32_e32 v246, v236, v246
	ds_write_b32 v233, v246 offset:50176
	s_waitcnt lgkmcnt(0)
	s_barrier
	v_readfirstlane_b32 s2, v1
	s_nop 3
	s_cmp_gt_u32 s2, 1
	s_cbranch_scc1 .Lmain_end
	v_and_b32_e32 v2, 31, v0
	v_lshlrev_b32_e32 v3, 5, v0
	v_and_b32_e32 v3, 0xc00, v3
	v_lshl_or_b32 v8, v2, 2, v3
	v_add_u32_e32 v8, 0xb800, v8
	ds_read2_b32 v[2:3], v8 offset1:32
	ds_read2_b32 v[4:5], v8 offset0:64 offset1:96
	ds_read2_b32 v[6:7], v8 offset0:128 offset1:160
	ds_read2_b32 v[10:11], v8 offset0:192 offset1:224
	s_mov_b32 s8, 0xf800000
	s_lshr_b32 s2, s30, 3
	s_lshl_b32 s2, s2, 7
	s_add_u32 s2, s2, 0x300000
	s_add_u32 s6, s6, s2
	s_addc_u32 s7, s7, 0
	s_mov_b32 s4, 0
	s_mov_b32 s5, 0x41d00000
	s_mov_b32 s16, 0
	s_mov_b32 s17, 0x420e0000
	s_waitcnt lgkmcnt(0)
	v_min3_f32 v2, v2, v3, v4
	v_min3_f32 v5, v5, v6, v7
	v_min3_f32 v2, v2, v10, v11
	v_min_f32_e32 v2, v2, v5
	s_waitcnt lgkmcnt(0)
	v_add_f32_e32 v20, v20, v21
	v_add_f32_e32 v22, v22, v23
	v_add_f32_e32 v24, v24, v25
	v_add_f32_e32 v26, v26, v27
	v_add_f32_e32 v28, v28, v29
	v_add_f32_e32 v30, v30, v31
	v_add_f32_e32 v32, v32, v33
	v_add_f32_e32 v34, v34, v35
	v_add_f32_e32 v20, v20, v22
	v_add_f32_e32 v24, v24, v26
	v_add_f32_e32 v28, v28, v30
	v_add_f32_e32 v32, v32, v34
	v_add_f32_e32 v20, v20, v24
	v_add_f32_e32 v28, v28, v32
	v_add_f32_e32 v20, v20, v28
	v_add_f32_e32 v2, v2, v20
	v_max_f32_e32 v2, 0, v2
	v_mul_f32_e32 v3, 0x4f800000, v2
	v_cmp_gt_f32_e32 vcc, s8, v2
	s_nop 1
	v_cndmask_b32_e32 v2, v2, v3, vcc
	v_sqrt_f32_e32 v3, v2
	s_nop 0
	v_add_u32_e32 v4, -1, v3
	v_fma_f32 v5, -v4, v3, v2
	v_cmp_ge_f32_e64 s[18:19], 0, v5
	v_add_u32_e32 v5, 1, v3
	s_nop 0
	v_cndmask_b32_e64 v4, v3, v4, s[18:19]
	v_fma_f32 v3, -v5, v3, v2
	v_cmp_lt_f32_e64 s[18:19], 0, v3
	s_nop 1
	v_cndmask_b32_e64 v3, v4, v5, s[18:19]
	v_mul_f32_e32 v4, 0x37800000, v3
	v_cndmask_b32_e32 v3, v3, v4, vcc
	v_mov_b32_e32 v4, 0x260
	v_cmp_class_f32_e32 vcc, v2, v4
	s_nop 1
	v_cndmask_b32_e32 v2, v3, v2, vcc
	s_nop 1
	v_add_f32_dpp v3, v2, v2 quad_perm:[1,0,3,2] row_mask:0xf bank_mask:0xf
	s_nop 1
	v_add_f32_dpp v4, v3, v3 quad_perm:[2,3,0,1] row_mask:0xf bank_mask:0xf
	s_nop 1
	v_add_f32_dpp v5, v4, v4 row_half_mirror row_mask:0xf bank_mask:0xf
	s_nop 1
	v_add_f32_dpp v6, v5, v5 row_mirror row_mask:0xf bank_mask:0xf
	s_nop 1
	v_readlane_b32 s12, v6, 0
	v_readlane_b32 s13, v6, 16
	v_readlane_b32 s14, v6, 32
	v_readlane_b32 s15, v6, 48
	s_nop 3
	v_mov_b32_e32 v7, s12
	v_add_f32_e32 v7, s13, v7
	v_mov_b32_e32 v9, s14
	v_add_f32_e32 v9, s15, v9
	v_add_f32_e32 v0, v7, v9
	v_mov_b32_e32 v4, 0
	s_mov_b64 exec, 1
	v_cvt_f64_f32_e32 v[6:7], v0
	v_add_f64 v[8:9], v[6:7], s[4:5]
	global_atomic_add_f64 v[10:11], v4, v[8:9], s[6:7] sc0
	s_waitcnt vmcnt(0)
	v_cmp_le_f64_e32 vcc, s[16:17], v[10:11]
	s_and_saveexec_b64 s[2:3], vcc
	s_cbranch_execz .Lmain_end
	v_add_f64 v[10:11], v[10:11], -s[16:17]
	v_add_f64 v[10:11], v[10:11], v[6:7]
	v_cvt_f32_f64_e32 v0, v[10:11]
	v_mul_f32_e32 v0, 0x38000000, v0
	global_atomic_add_f32 v4, v0, s[10:11]
